# P7 prologue: the first unit's four token-index gathers requested together and awaited once
# baseline (speedup 1.0000x reference)
; template <class Epi, bool G1> ...
;     ...
;     int RA[2], CA[2];
; #pragma unroll
;     for (int i = 0; i < 2; ++i) stage_rc(tid * 16 + i * 8192, RA[i], CA[i]);
;     const unsigned ldsw = (unsigned)wid * 1024u;
;     const int aoff = lds_byte(wr * 64 + fr, fq * 8), boff = lds_byte(wc * 32 + fr, fq * 8);
;     const int hfB = wid >> 2, kgB = (tid >> 5) & 7, ngB = tid & 31, g8 = ngB & 7;
;     const int wB0 = lds_byte(32 * (ngB >> 3) + (g8 & 1) * 16 + (g8 >> 1) * 4, 8 * kgB);
;     ...
;     MG_ROWS(cur, rowC); const float* bC = MG_BPTR(cur); bool bact = MG_BACT(cur);
.LBB0_1036:
	v_lshl_add_u32 v0, s24, 6, v24
	v_bfe_i32 v2, v0, 27, 1
	v_lshlrev_b32_e32 v3, 4, v0
	v_lshrrev_b32_e32 v2, 22, v2
	v_add_u32_e32 v2, v3, v2
	v_and_b32_e32 v2, 0xfffffc00, v2
	v_sub_u32_e32 v2, v3, v2
	v_ashrrev_i32_e32 v1, 31, v0
	v_lshrrev_b32_e32 v4, 4, v2
	s_add_u32 s16, s2, 0x1000000
	v_lshrrev_b32_e32 v1, 26, v1
	v_bitop3_b32 v2, v4, v2, 32 bitop3:0x6c
	s_addc_u32 s17, s3, 0
	v_add_u32_e32 v1, v0, v1
	v_ashrrev_i32_e32 v5, 31, v2
	s_ashr_i32 s12, s50, 3
	v_ashrrev_i32_e32 v1, 6, v1
	v_lshrrev_b32_e32 v5, 26, v5
	s_lshl_b32 s13, s12, 2
	v_lshlrev_b32_e32 v4, 3, v1
	v_add_u32_e32 v5, v2, v5
	s_add_i32 s13, s13, 0
	v_and_b32_e32 v4, -16, v4
	v_ashrrev_i32_e32 v6, 6, v5
	s_add_i32 s14, s13, 0x20000
	s_add_i32 s13, s13, 0x20200
	v_add_u32_e32 v214, v6, v4
	v_and_b32_e32 v4, 0xc0, v5
	v_mov_b32_e32 v5, s14
	v_mov_b32_e32 v6, s13
	ds_read_b32 v5, v5
	ds_read_b32 v6, v6
	v_lshlrev_b32_e32 v1, 5, v1
	v_sub_u32_e32 v2, v2, v4
	v_mov_b32_e32 v4, 1
	v_and_b32_e32 v1, 32, v1
	v_ashrrev_i16_sdwa v2, v4, sext(v2) dst_sel:DWORD dst_unused:UNUSED_PAD src0_sel:DWORD src1_sel:BYTE_0
	s_lshl_b32 s13, s49, 8
	s_lshl_b32 s14, s12, 14
	v_add_u32_sdwa v25, v1, sext(v2) dst_sel:DWORD dst_unused:UNUSED_PAD src0_sel:DWORD src1_sel:WORD_0
	s_waitcnt lgkmcnt(0)
	v_add_u32_e32 v2, v6, v5
	v_sub_u32_e32 v1, s14, v5
	v_add_u32_e32 v5, s13, v214
	v_cmp_lt_i32_e32 vcc, v5, v2
	v_mov_b32_e32 v192, -1
	v_mov_b32_e32 v194, -1
	s_and_saveexec_b64 s[14:15], vcc
	s_cbranch_execz .LBB0_1038
	v_add_u32_e32 v6, v1, v5
	v_ashrrev_i32_e32 v7, 31, v6
	v_lshl_add_u64 v[6:7], v[6:7], 2, s[16:17]
	global_load_dword v194, v[6:7], off
.LBB0_1038:
	s_or_b64 exec, exec, s[14:15]
	v_add_u32_e32 v3, 0x2000, v3
	v_ashrrev_i32_e32 v5, 31, v3
	v_lshrrev_b32_e32 v5, 22, v5
	v_add_u32_e32 v5, v3, v5
	v_ashrrev_i32_e32 v5, 10, v5
	v_mul_i32_i24_e32 v6, 0x400, v5
	v_sub_u32_e32 v3, v3, v6
	v_lshrrev_b32_e32 v6, 4, v3
	v_bitop3_b32 v3, v6, v3, 32 bitop3:0x6c
	v_ashrrev_i32_e32 v7, 31, v3
	v_lshrrev_b32_e32 v7, 26, v7
	v_lshlrev_b32_e32 v6, 3, v5
	v_add_u32_e32 v7, v3, v7
	v_and_b32_e32 v6, -16, v6
	v_ashrrev_i32_e32 v8, 6, v7
	v_add_u32_e32 v215, v8, v6
	v_and_b32_e32 v6, 0xc0, v7
	v_lshlrev_b32_e32 v5, 5, v5
	v_sub_u32_e32 v3, v3, v6
	v_and_b32_e32 v5, 32, v5
	v_ashrrev_i16_sdwa v3, v4, sext(v3) dst_sel:DWORD dst_unused:UNUSED_PAD src0_sel:DWORD src1_sel:BYTE_0
	v_add_u32_sdwa v26, v5, sext(v3) dst_sel:DWORD dst_unused:UNUSED_PAD src0_sel:DWORD src1_sel:WORD_0
	v_add_u32_e32 v3, s13, v215
	v_cmp_lt_i32_e32 vcc, v3, v2
	s_and_saveexec_b64 s[14:15], vcc
	s_cbranch_execz .LBB0_1040
	v_add_u32_e32 v4, v1, v3
	v_ashrrev_i32_e32 v5, 31, v4
	v_lshl_add_u64 v[4:5], v[4:5], 2, s[16:17]
	global_load_dword v192, v[4:5], off
.LBB0_1040:
	s_or_b64 exec, exec, s[14:15]
	s_bitset1_b32 s13, 7
	v_add_u32_e32 v3, s13, v214
	v_cmp_lt_i32_e32 vcc, v3, v2
	v_mov_b32_e32 v196, -1
	v_mov_b32_e32 v198, -1
	s_and_saveexec_b64 s[14:15], vcc
	s_cbranch_execz .LBB0_1042
	v_add_u32_e32 v4, v1, v3
	v_ashrrev_i32_e32 v5, 31, v4
	v_lshl_add_u64 v[4:5], v[4:5], 2, s[16:17]
	global_load_dword v198, v[4:5], off
.LBB0_1042:
	s_or_b64 exec, exec, s[14:15]
	v_add_u32_e32 v3, s13, v215
	v_cmp_lt_i32_e32 vcc, v3, v2
	s_and_saveexec_b64 s[14:15], vcc
	s_cbranch_execz .LBB0_1044
	v_add_u32_e32 v2, v1, v3
	v_ashrrev_i32_e32 v3, 31, v2
	v_lshl_add_u64 v[2:3], v[2:3], 2, s[16:17]
	global_load_dword v196, v[2:3], off
.LBB0_1044:
	s_or_b64 exec, exec, s[14:15]
	s_waitcnt vmcnt(0)
	v_cmp_ne_u32_e32 vcc, -1, v194
	v_lshlrev_b32_e32 v6, 11, v194
	v_and_b32_e32 v6, 0xfffff000, v6
	v_lshl_add_u32 v6, v25, 1, v6
	v_cndmask_b32_e32 v194, v194, v6, vcc
	v_cmp_ne_u32_e32 vcc, -1, v192
	v_lshlrev_b32_e32 v6, 11, v192
	v_and_b32_e32 v6, 0xfffff000, v6
	v_lshl_add_u32 v6, v26, 1, v6
	v_cndmask_b32_e32 v192, v192, v6, vcc
	v_cmp_ne_u32_e32 vcc, -1, v198
	v_lshlrev_b32_e32 v6, 11, v198
	v_and_b32_e32 v6, 0xfffff000, v6
	v_lshl_add_u32 v6, v25, 1, v6
	v_cndmask_b32_e32 v198, v198, v6, vcc
	v_cmp_ne_u32_e32 vcc, -1, v196
	v_lshlrev_b32_e32 v6, 11, v196
	v_and_b32_e32 v6, 0xfffff000, v6
	v_lshl_add_u32 v6, v26, 1, v6
	v_cndmask_b32_e32 v196, v196, v6, vcc
	v_and_b32_e32 v27, 31, v24
	v_bfe_u32 v216, v24, 3, 2
	s_cmp_lt_i32 s48, 0
	s_mov_b64 s[20:21], -1
	s_cbranch_scc1 .LBB0_1049
	s_cmp_gt_u32 s48, 3
	s_cbranch_scc0 .LBB0_1047
	v_lshrrev_b32_e32 v1, 4, v27
	s_add_i32 s13, s48, -4
	v_cmp_eq_u32_e64 s[20:21], s13, v1
	s_cbranch_execz .LBB0_1048
	s_branch .LBB0_1049
